# P4 per-token fp4 row conversion hand-written, row loads requested early (row A at token top, row B behind the attention steps), compiled conversion loop removed
# speedup vs baseline: 1.0083x; 1.0083x over previous
.LBB0_520:
	s_cmp_gt_i32 s42, 0x3fff
	s_cbranch_scc1 .Lcv_a_noi
	s_lshl_b32 s20, s42, 14
	s_add_u32 s20, s48, s20
	s_addc_u32 s21, s49, 0
	v_lshlrev_b32_e32 v138, 4, v1
	global_load_dwordx4 v[180:183], v138, s[20:21] nt
	global_load_dwordx4 v[184:187], v138, s[20:21] offset:1024 nt
	global_load_dwordx4 v[188:191], v138, s[20:21] offset:2048 nt
	global_load_dwordx4 v[192:195], v138, s[20:21] offset:3072 nt
	s_add_u32 s20, s20, 0x1000
	s_addc_u32 s21, s21, 0
	global_load_dwordx4 v[196:199], v138, s[20:21] nt
	global_load_dwordx4 v[200:203], v138, s[20:21] offset:1024 nt
	global_load_dwordx4 v[204:207], v138, s[20:21] offset:2048 nt
	global_load_dwordx4 v[208:211], v138, s[20:21] offset:3072 nt
	s_add_u32 s20, s20, 0x1000
	s_addc_u32 s21, s21, 0
	global_load_dwordx4 v[212:215], v138, s[20:21] nt
	global_load_dwordx4 v[216:219], v138, s[20:21] offset:1024 nt
	global_load_dwordx4 v[220:223], v138, s[20:21] offset:2048 nt
	global_load_dwordx4 v[224:227], v138, s[20:21] offset:3072 nt
	s_add_u32 s20, s20, 0x1000
	s_addc_u32 s21, s21, 0
	global_load_dwordx4 v[228:231], v138, s[20:21] nt
	global_load_dwordx4 v[232:235], v138, s[20:21] offset:1024 nt
	global_load_dwordx4 v[236:239], v138, s[20:21] offset:2048 nt
	global_load_dwordx4 v[134:137], v138, s[20:21] offset:3072 nt

.LBB0_1123:
	s_or_b64 exec, exec, s[2:3]
	s_cmp_gt_i32 s42, 0x3fff
	s_cbranch_scc1 .Lcv_a_nop
	s_waitcnt vmcnt(0)
	v_pk_mul_f32 v[50:51], v[180:181], v[180:181]
	v_pk_mul_f32 v[52:53], v[182:183], v[182:183]
	v_pk_fma_f32 v[50:51], v[184:185], v[184:185], v[50:51]
	v_pk_fma_f32 v[52:53], v[186:187], v[186:187], v[52:53]
	v_pk_fma_f32 v[50:51], v[188:189], v[188:189], v[50:51]
	v_pk_fma_f32 v[52:53], v[190:191], v[190:191], v[52:53]
	v_pk_fma_f32 v[50:51], v[192:193], v[192:193], v[50:51]
	v_pk_fma_f32 v[52:53], v[194:195], v[194:195], v[52:53]
	v_pk_fma_f32 v[50:51], v[196:197], v[196:197], v[50:51]
	v_pk_fma_f32 v[52:53], v[198:199], v[198:199], v[52:53]
	v_pk_fma_f32 v[50:51], v[200:201], v[200:201], v[50:51]
	v_pk_fma_f32 v[52:53], v[202:203], v[202:203], v[52:53]
	v_pk_fma_f32 v[50:51], v[204:205], v[204:205], v[50:51]
	v_pk_fma_f32 v[52:53], v[206:207], v[206:207], v[52:53]
	v_pk_fma_f32 v[50:51], v[208:209], v[208:209], v[50:51]
	v_pk_fma_f32 v[52:53], v[210:211], v[210:211], v[52:53]
	v_pk_fma_f32 v[50:51], v[212:213], v[212:213], v[50:51]
	v_pk_fma_f32 v[52:53], v[214:215], v[214:215], v[52:53]
	v_pk_fma_f32 v[50:51], v[216:217], v[216:217], v[50:51]
	v_pk_fma_f32 v[52:53], v[218:219], v[218:219], v[52:53]
	v_pk_fma_f32 v[50:51], v[220:221], v[220:221], v[50:51]
	v_pk_fma_f32 v[52:53], v[222:223], v[222:223], v[52:53]
	v_pk_fma_f32 v[50:51], v[224:225], v[224:225], v[50:51]
	v_pk_fma_f32 v[52:53], v[226:227], v[226:227], v[52:53]
	v_pk_fma_f32 v[50:51], v[228:229], v[228:229], v[50:51]
	v_pk_fma_f32 v[52:53], v[230:231], v[230:231], v[52:53]
	v_pk_fma_f32 v[50:51], v[232:233], v[232:233], v[50:51]
	v_pk_fma_f32 v[52:53], v[234:235], v[234:235], v[52:53]
	v_pk_fma_f32 v[50:51], v[236:237], v[236:237], v[50:51]
	v_pk_fma_f32 v[52:53], v[238:239], v[238:239], v[52:53]
	v_pk_fma_f32 v[50:51], v[134:135], v[134:135], v[50:51]
	v_pk_fma_f32 v[52:53], v[136:137], v[136:137], v[52:53]
	v_pk_add_f32 v[50:51], v[50:51], v[52:53]
	v_add_f32_e32 v54, v50, v51
	s_nop 1
	v_add_f32_dpp v54, v54, v54 quad_perm:[1,0,3,2] row_mask:0xf bank_mask:0xf bound_ctrl:1
	s_nop 1
	v_add_f32_dpp v54, v54, v54 quad_perm:[2,3,0,1] row_mask:0xf bank_mask:0xf bound_ctrl:1
	s_nop 1
	v_add_f32_dpp v54, v54, v54 row_half_mirror row_mask:0xf bank_mask:0xf bound_ctrl:1
	s_nop 1
	v_add_f32_dpp v54, v54, v54 row_mirror row_mask:0xf bank_mask:0xf bound_ctrl:1
	s_nop 1
	v_add_f32_dpp v54, v54, v54 row_bcast:15 row_mask:0xa bank_mask:0xf
	s_nop 1
	v_add_f32_dpp v54, v54, v54 row_bcast:31 row_mask:0xc bank_mask:0xf
	s_nop 1
	v_readlane_b32 s22, v54, 63
	s_lshl_b32 s24, s42, 11
	v_readlane_b32 s26, v242, 33
	v_readlane_b32 s27, v242, 34
	s_add_u32 s23, s42, 0x4000
	s_lshl_b32 s23, s23, 2
	v_mov_b32_e32 v56, s22
	v_mul_f32_e32 v56, 0x39800000, v56
	v_sqrt_f32_e32 v56, v56
	v_cmp_lt_f32_e64 s[28:29], 0, s22
	v_mul_f32_e32 v56, 0x3eddddde, v56
	s_add_u32 s26, s26, s24
	s_addc_u32 s27, s27, 0
	v_cndmask_b32_e64 v56, 1.0, v56, s[28:29]
	s_add_u32 s24, s74, s23
	s_addc_u32 s25, s75, 0
	v_rcp_f32_e32 v58, v56
	v_mov_b32_e32 v54, 0
	v_fma_f32 v59, -v56, v58, 1.0
	v_fmac_f32_e32 v58, v59, v58
	s_mov_b64 exec, 1
	global_store_dword v54, v56, s[24:25]
	s_mov_b64 exec, -1
	v_lshlrev_b32_e32 v138, 4, v1
	v_pk_mul_f32 v[180:181], v[180:181], v[58:59] op_sel_hi:[1,0]
	v_pk_mul_f32 v[182:183], v[182:183], v[58:59] op_sel_hi:[1,0]
	v_pk_mul_f32 v[184:185], v[184:185], v[58:59] op_sel_hi:[1,0]
	v_pk_mul_f32 v[186:187], v[186:187], v[58:59] op_sel_hi:[1,0]
	v_pk_mul_f32 v[188:189], v[188:189], v[58:59] op_sel_hi:[1,0]
	v_pk_mul_f32 v[190:191], v[190:191], v[58:59] op_sel_hi:[1,0]
	v_pk_mul_f32 v[192:193], v[192:193], v[58:59] op_sel_hi:[1,0]
	v_pk_mul_f32 v[194:195], v[194:195], v[58:59] op_sel_hi:[1,0]
	v_pk_mul_f32 v[196:197], v[196:197], v[58:59] op_sel_hi:[1,0]
	v_pk_mul_f32 v[198:199], v[198:199], v[58:59] op_sel_hi:[1,0]
	v_pk_mul_f32 v[200:201], v[200:201], v[58:59] op_sel_hi:[1,0]
	v_pk_mul_f32 v[202:203], v[202:203], v[58:59] op_sel_hi:[1,0]
	v_pk_mul_f32 v[204:205], v[204:205], v[58:59] op_sel_hi:[1,0]
	v_pk_mul_f32 v[206:207], v[206:207], v[58:59] op_sel_hi:[1,0]
	v_pk_mul_f32 v[208:209], v[208:209], v[58:59] op_sel_hi:[1,0]
	v_pk_mul_f32 v[210:211], v[210:211], v[58:59] op_sel_hi:[1,0]
	v_pk_mul_f32 v[212:213], v[212:213], v[58:59] op_sel_hi:[1,0]
	v_pk_mul_f32 v[214:215], v[214:215], v[58:59] op_sel_hi:[1,0]
	v_pk_mul_f32 v[216:217], v[216:217], v[58:59] op_sel_hi:[1,0]
	v_pk_mul_f32 v[218:219], v[218:219], v[58:59] op_sel_hi:[1,0]
	v_pk_mul_f32 v[220:221], v[220:221], v[58:59] op_sel_hi:[1,0]
	v_pk_mul_f32 v[222:223], v[222:223], v[58:59] op_sel_hi:[1,0]
	v_pk_mul_f32 v[224:225], v[224:225], v[58:59] op_sel_hi:[1,0]
	v_pk_mul_f32 v[226:227], v[226:227], v[58:59] op_sel_hi:[1,0]
	v_pk_mul_f32 v[228:229], v[228:229], v[58:59] op_sel_hi:[1,0]
	v_pk_mul_f32 v[230:231], v[230:231], v[58:59] op_sel_hi:[1,0]
	v_pk_mul_f32 v[232:233], v[232:233], v[58:59] op_sel_hi:[1,0]
	v_pk_mul_f32 v[234:235], v[234:235], v[58:59] op_sel_hi:[1,0]
	v_pk_mul_f32 v[236:237], v[236:237], v[58:59] op_sel_hi:[1,0]
	v_pk_mul_f32 v[238:239], v[238:239], v[58:59] op_sel_hi:[1,0]
	v_pk_mul_f32 v[134:135], v[134:135], v[58:59] op_sel_hi:[1,0]
	v_pk_mul_f32 v[136:137], v[136:137], v[58:59] op_sel_hi:[1,0]
	v_cvt_scalef32_pk_fp4_f32 v60, v180, v181, 1.0
	v_cvt_scalef32_pk_fp4_f32 v61, v188, v189, 1.0
	v_cvt_scalef32_pk_fp4_f32 v62, v196, v197, 1.0
	v_cvt_scalef32_pk_fp4_f32 v63, v204, v205, 1.0
	v_cvt_scalef32_pk_fp4_f32 v60, v182, v183, 1.0 op_sel:[0,0,1,0]
	v_cvt_scalef32_pk_fp4_f32 v61, v190, v191, 1.0 op_sel:[0,0,1,0]
	v_cvt_scalef32_pk_fp4_f32 v62, v198, v199, 1.0 op_sel:[0,0,1,0]
	v_cvt_scalef32_pk_fp4_f32 v63, v206, v207, 1.0 op_sel:[0,0,1,0]
	v_cvt_scalef32_pk_fp4_f32 v60, v184, v185, 1.0 op_sel:[0,0,0,1]
	v_cvt_scalef32_pk_fp4_f32 v61, v192, v193, 1.0 op_sel:[0,0,0,1]
	v_cvt_scalef32_pk_fp4_f32 v62, v200, v201, 1.0 op_sel:[0,0,0,1]
	v_cvt_scalef32_pk_fp4_f32 v63, v208, v209, 1.0 op_sel:[0,0,0,1]
	v_cvt_scalef32_pk_fp4_f32 v60, v186, v187, 1.0 op_sel:[0,0,1,1]
	v_cvt_scalef32_pk_fp4_f32 v61, v194, v195, 1.0 op_sel:[0,0,1,1]
	v_cvt_scalef32_pk_fp4_f32 v62, v202, v203, 1.0 op_sel:[0,0,1,1]
	v_cvt_scalef32_pk_fp4_f32 v63, v210, v211, 1.0 op_sel:[0,0,1,1]
	s_nop 0
	global_store_dwordx4 v138, v[60:63], s[26:27]
	s_nop 1
	v_cvt_scalef32_pk_fp4_f32 v60, v212, v213, 1.0
	v_cvt_scalef32_pk_fp4_f32 v61, v220, v221, 1.0
	v_cvt_scalef32_pk_fp4_f32 v62, v228, v229, 1.0
	v_cvt_scalef32_pk_fp4_f32 v63, v236, v237, 1.0
	v_cvt_scalef32_pk_fp4_f32 v60, v214, v215, 1.0 op_sel:[0,0,1,0]
	v_cvt_scalef32_pk_fp4_f32 v61, v222, v223, 1.0 op_sel:[0,0,1,0]
	v_cvt_scalef32_pk_fp4_f32 v62, v230, v231, 1.0 op_sel:[0,0,1,0]
	v_cvt_scalef32_pk_fp4_f32 v63, v238, v239, 1.0 op_sel:[0,0,1,0]
	v_cvt_scalef32_pk_fp4_f32 v60, v216, v217, 1.0 op_sel:[0,0,0,1]
	v_cvt_scalef32_pk_fp4_f32 v61, v224, v225, 1.0 op_sel:[0,0,0,1]
	v_cvt_scalef32_pk_fp4_f32 v62, v232, v233, 1.0 op_sel:[0,0,0,1]
	v_cvt_scalef32_pk_fp4_f32 v63, v134, v135, 1.0 op_sel:[0,0,0,1]
	v_cvt_scalef32_pk_fp4_f32 v60, v218, v219, 1.0 op_sel:[0,0,1,1]
	v_cvt_scalef32_pk_fp4_f32 v61, v226, v227, 1.0 op_sel:[0,0,1,1]
	v_cvt_scalef32_pk_fp4_f32 v62, v234, v235, 1.0 op_sel:[0,0,1,1]
	v_cvt_scalef32_pk_fp4_f32 v63, v136, v137, 1.0 op_sel:[0,0,1,1]
	s_nop 0
	global_store_dwordx4 v138, v[60:63], s[26:27] offset:1024
.Lcv_a_nop:
	s_waitcnt lgkmcnt(0)
	v_add_u32_e32 v2, 31, v172
	v_and_b32_e32 v173, 15, v151
	v_ashrrev_i32_e32 v174, 4, v151
	v_ashrrev_i32_e32 v176, 5, v2
	v_mov_b32_e32 v29, 0
	v_lshlrev_b32_e32 v148, 7, v173
	v_mov_b32_e32 v149, v147
	v_cmp_lt_i32_e32 vcc, 0, v176
	v_lshlrev_b32_e32 v150, 2, v174
	v_mov_b32_e32 v28, v29
	v_mov_b32_e32 v27, v29
	v_mov_b32_e32 v26, v29
	v_mov_b32_e32 v33, v29
	v_mov_b32_e32 v32, v29
	v_mov_b32_e32 v31, v29
	v_mov_b32_e32 v30, v29
	v_mov_b32_e32 v25, v29
	v_mov_b32_e32 v24, v29
	v_mov_b32_e32 v23, v29
	v_mov_b32_e32 v22, v29
	v_mov_b32_e32 v21, v29
	v_mov_b32_e32 v20, v29
	v_mov_b32_e32 v19, v29
	v_mov_b32_e32 v18, v29
	v_mov_b32_e32 v17, v29
	v_mov_b32_e32 v16, v29
	v_mov_b32_e32 v15, v29
	v_mov_b32_e32 v14, v29
	v_mov_b32_e32 v13, v29
	v_mov_b32_e32 v12, v29
	v_mov_b32_e32 v11, v29
	v_mov_b32_e32 v10, v29
	v_mov_b32_e32 v9, v29
	v_mov_b32_e32 v8, v29
	v_mov_b32_e32 v7, v29
	v_mov_b32_e32 v6, v29
	v_mov_b32_e32 v5, v29
	v_mov_b32_e32 v4, v29
	v_mov_b32_e32 v3, v29
	v_mov_b32_e32 v2, v29
	v_mov_b32_e32 v179, v29
	s_and_saveexec_b64 s[0:1], vcc
	s_cbranch_execz .LBB0_1127
	v_readfirstlane_b32 s10, v176
	v_readfirstlane_b32 s36, v172
	v_readlane_b32 s37, v242, 49
	s_mul_i32 s5, s78, 0x3400000
	s_mul_hi_i32 s4, s78, 0x3400000
	s_add_u32 s2, s82, s5
	s_addc_u32 s3, s83, s4
	s_add_u32 s4, s2, 0x2800
	s_addc_u32 s5, s3, 0
	s_add_u32 s6, s2, 0x2900
	s_addc_u32 s7, s3, 0
	s_mul_i32 s20, s97, 0x3400
	s_mul_hi_u32 s21, s96, 0x3400
	s_add_i32 s21, s21, s20
	s_mul_i32 s20, s96, 0x3400
	s_add_u32 s20, s82, s20
	s_addc_u32 s21, s83, s21
	s_add_u32 s20, s20, 0x1800
	s_addc_u32 s21, s21, 0
	s_add_u32 s26, s89, 0x400
	s_lshl_b32 s27, s37, 13
	s_add_u32 s27, s27, 0x14000
	s_sub_u32 s37, s27, s26
	v_lshlrev_b32_e32 v152, 2, v150
	v_lshl_add_u32 v153, v148, 1, v152
	global_load_dwordx4 v[42:45], v153, s[20:21]
	global_load_dwordx4 v[34:37], v153, s[20:21] offset:64
	global_load_dwordx4 v[38:41], v153, s[20:21] offset:128
	global_load_dwordx4 v[46:49], v153, s[20:21] offset:192
	v_lshl_add_u32 v110, v173, 2, s89
	v_add_u32_e32 v111, s89, v150
	ds_read2_b32 v[98:99], v110 offset0:0 offset1:16
	ds_read2_b32 v[100:101], v111 offset0:0 offset1:4
	ds_read2_b32 v[102:103], v111 offset0:8 offset1:12
	ds_read2_b32 v[104:105], v111 offset0:16 offset1:20
	ds_read2_b32 v[106:107], v111 offset0:24 offset1:28
	v_lshlrev_b32_e32 v112, 1, v174
	v_xor_b32_e32 v112, v112, v173
	v_lshlrev_b32_e32 v177, 4, v112
	v_xor_b32_e32 v178, 0x80, v177
	v_lshrrev_b32_e32 v112, 2, v173
	v_add_u32_e32 v112, v112, v150
	v_and_b32_e32 v113, 7, v112
	v_and_b32_e32 v96, 3, v173
	v_lshlrev_b32_e32 v96, 3, v96
	v_lshl_add_u32 v112, v112, 8, v96
	v_add_u32_e32 v112, s26, v112
	v_xor_b32_e32 v96, 0, v113
	v_lshl_add_u32 v188, v96, 5, v112
	v_xor_b32_e32 v96, 1, v113
	v_lshl_add_u32 v189, v96, 5, v112
	v_xor_b32_e32 v96, 2, v113
	v_lshl_add_u32 v190, v96, 5, v112
	v_xor_b32_e32 v96, 3, v113
	v_lshl_add_u32 v191, v96, 5, v112
	v_xor_b32_e32 v96, 4, v113
	v_lshl_add_u32 v192, v96, 5, v112
	v_xor_b32_e32 v96, 5, v113
	v_lshl_add_u32 v193, v96, 5, v112
	v_xor_b32_e32 v96, 6, v113
	v_lshl_add_u32 v194, v96, 5, v112
	v_xor_b32_e32 v96, 7, v113
	v_lshl_add_u32 v195, v96, 5, v112
	v_add_u32_e32 v196, s37, v188
	v_add_u32_e32 v197, s37, v189
	v_add_u32_e32 v198, s37, v190
	v_add_u32_e32 v199, s37, v191
	v_add_u32_e32 v200, s37, v192
	v_add_u32_e32 v201, s37, v193
	v_add_u32_e32 v202, s37, v194
	v_add_u32_e32 v203, s37, v195
	v_mov_b32_e32 v2, 0
	v_mov_b32_e32 v3, 0
	v_mov_b32_e32 v4, 0
	v_mov_b32_e32 v5, 0
	v_mov_b32_e32 v6, 0
	v_mov_b32_e32 v7, 0
	v_mov_b32_e32 v8, 0
	v_mov_b32_e32 v9, 0
	v_mov_b32_e32 v10, 0
	v_mov_b32_e32 v11, 0
	v_mov_b32_e32 v12, 0
	v_mov_b32_e32 v13, 0
	v_mov_b32_e32 v14, 0
	v_mov_b32_e32 v15, 0
	v_mov_b32_e32 v16, 0
	v_mov_b32_e32 v17, 0
	v_mov_b32_e32 v18, 0
	v_mov_b32_e32 v19, 0
	v_mov_b32_e32 v20, 0
	v_mov_b32_e32 v21, 0
	v_mov_b32_e32 v22, 0
	v_mov_b32_e32 v23, 0
	v_mov_b32_e32 v24, 0
	v_mov_b32_e32 v25, 0
	v_mov_b32_e32 v26, 0
	v_mov_b32_e32 v27, 0
	v_mov_b32_e32 v28, 0
	v_mov_b32_e32 v29, 0
	v_mov_b32_e32 v30, 0
	v_mov_b32_e32 v31, 0
	v_mov_b32_e32 v32, 0
	v_mov_b32_e32 v33, 0
	v_mov_b32_e32 v179, 0
	v_mov_b32_e32 v181, 0xf149f2ca
	v_mov_b32_e32 v95, 0
	s_mov_b32 s11, 0
	s_mov_b32 s22, 0
	s_waitcnt lgkmcnt(0)
	v_mad_u32_u24 v108, v98, s35, v152
	v_mad_u32_u24 v109, v99, s35, v152
	global_load_dwordx4 v[50:53], v108, s[4:5]
	global_load_dwordx4 v[66:69], v109, s[4:5]
	global_load_dwordx4 v[54:57], v108, s[4:5] offset:64
	global_load_dwordx4 v[70:73], v109, s[4:5] offset:64
	global_load_dwordx4 v[58:61], v108, s[4:5] offset:128
	global_load_dwordx4 v[74:77], v109, s[4:5] offset:128
	global_load_dwordx4 v[62:65], v108, s[4:5] offset:192
	global_load_dwordx4 v[78:81], v109, s[4:5] offset:192
	s_mov_b32 m0, s26
	v_mad_u32_u24 v108, v100, s35, v177
	global_load_lds_dwordx4 v108, s[6:7]
	s_add_u32 m0, s26, 1024
	v_mad_u32_u24 v108, v101, s35, v178
	global_load_lds_dwordx4 v108, s[6:7]
	s_add_u32 m0, s26, 2048
	v_mad_u32_u24 v108, v102, s35, v177
	global_load_lds_dwordx4 v108, s[6:7]
	s_add_u32 m0, s26, 3072
	v_mad_u32_u24 v108, v103, s35, v178
	global_load_lds_dwordx4 v108, s[6:7]
	s_add_u32 m0, s26, 4096
	v_mad_u32_u24 v108, v104, s35, v177
	global_load_lds_dwordx4 v108, s[6:7]
	s_add_u32 m0, s26, 5120
	v_mad_u32_u24 v108, v105, s35, v178
	global_load_lds_dwordx4 v108, s[6:7]
	s_add_u32 m0, s26, 6144
	v_mad_u32_u24 v108, v106, s35, v177
	global_load_lds_dwordx4 v108, s[6:7]
	s_add_u32 m0, s26, 7168
	v_mad_u32_u24 v108, v107, s35, v178
	global_load_lds_dwordx4 v108, s[6:7]
	s_cmp_ge_u32 s10, 2
	s_cbranch_scc0 .Lat_A
	ds_read2_b32 v[98:99], v110 offset0:32 offset1:48
	ds_read2_b32 v[100:101], v111 offset0:32 offset1:36
	ds_read2_b32 v[102:103], v111 offset0:40 offset1:44
	ds_read2_b32 v[104:105], v111 offset0:48 offset1:52
	ds_read2_b32 v[106:107], v111 offset0:56 offset1:60
	s_waitcnt lgkmcnt(0)
	v_mad_u32_u24 v108, v98, s35, v152
	v_mad_u32_u24 v109, v99, s35, v152
	global_load_dwordx4 v[114:117], v108, s[4:5]
	global_load_dwordx4 v[130:133], v109, s[4:5]
	global_load_dwordx4 v[118:121], v108, s[4:5] offset:64
	global_load_dwordx4 v[134:137], v109, s[4:5] offset:64
	global_load_dwordx4 v[122:125], v108, s[4:5] offset:128
	global_load_dwordx4 v[138:141], v109, s[4:5] offset:128
	global_load_dwordx4 v[126:129], v108, s[4:5] offset:192
	global_load_dwordx4 v[142:145], v109, s[4:5] offset:192
	s_mov_b32 m0, s27
	v_mad_u32_u24 v108, v100, s35, v177
	global_load_lds_dwordx4 v108, s[6:7]
	s_add_u32 m0, s27, 1024
	v_mad_u32_u24 v108, v101, s35, v178
	global_load_lds_dwordx4 v108, s[6:7]
	s_add_u32 m0, s27, 2048
	v_mad_u32_u24 v108, v102, s35, v177
	global_load_lds_dwordx4 v108, s[6:7]
	s_add_u32 m0, s27, 3072
	v_mad_u32_u24 v108, v103, s35, v178
	global_load_lds_dwordx4 v108, s[6:7]
	s_add_u32 m0, s27, 4096
	v_mad_u32_u24 v108, v104, s35, v177
	global_load_lds_dwordx4 v108, s[6:7]
	s_add_u32 m0, s27, 5120
	v_mad_u32_u24 v108, v105, s35, v178
	global_load_lds_dwordx4 v108, s[6:7]
	s_add_u32 m0, s27, 6144
	v_mad_u32_u24 v108, v106, s35, v177
	global_load_lds_dwordx4 v108, s[6:7]
	s_add_u32 m0, s27, 7168
	v_mad_u32_u24 v108, v107, s35, v178
	global_load_lds_dwordx4 v108, s[6:7]

.LBB0_1127:
	s_or_b64 exec, exec, s[0:1]
	s_add_i32 s30, s42, s40
	s_cmp_gt_i32 s30, 0x3fff
	s_cbranch_scc1 .Lcv_b_noi
	s_lshl_b32 s20, s30, 14
	s_add_u32 s20, s48, s20
	s_addc_u32 s21, s49, 0
	v_lshlrev_b32_e32 v138, 4, v1
	global_load_dwordx4 v[180:183], v138, s[20:21] nt
	global_load_dwordx4 v[184:187], v138, s[20:21] offset:1024 nt
	global_load_dwordx4 v[188:191], v138, s[20:21] offset:2048 nt
	global_load_dwordx4 v[192:195], v138, s[20:21] offset:3072 nt
	s_add_u32 s20, s20, 0x1000
	s_addc_u32 s21, s21, 0
	global_load_dwordx4 v[196:199], v138, s[20:21] nt
	global_load_dwordx4 v[200:203], v138, s[20:21] offset:1024 nt
	global_load_dwordx4 v[204:207], v138, s[20:21] offset:2048 nt
	global_load_dwordx4 v[208:211], v138, s[20:21] offset:3072 nt
	s_add_u32 s20, s20, 0x1000
	s_addc_u32 s21, s21, 0
	global_load_dwordx4 v[212:215], v138, s[20:21] nt
	global_load_dwordx4 v[216:219], v138, s[20:21] offset:1024 nt
	global_load_dwordx4 v[220:223], v138, s[20:21] offset:2048 nt
	global_load_dwordx4 v[224:227], v138, s[20:21] offset:3072 nt
	s_add_u32 s20, s20, 0x1000
	s_addc_u32 s21, s21, 0
	global_load_dwordx4 v[228:231], v138, s[20:21] nt
	global_load_dwordx4 v[232:235], v138, s[20:21] offset:1024 nt
	global_load_dwordx4 v[236:239], v138, s[20:21] offset:2048 nt
	global_load_dwordx4 v[134:137], v138, s[20:21] offset:3072 nt

.LBB0_1129:
	s_or_b64 exec, exec, s[4:5]
	v_div_scale_f32 v37, s[4:5], v36, v36, s13
	v_rcp_f32_e32 v38, v37
	v_ashrrev_i32_e32 v151, 31, v150
	v_mov_b32_e32 v43, v147
	v_mov_b32_e32 v78, v1
	v_fma_f32 v39, -v37, v38, 1.0
	v_fmac_f32_e32 v38, v39, v38
	v_div_scale_f32 v39, vcc, s13, v36, s13
	v_mul_f32_e32 v40, v39, v38
	v_fma_f32 v41, -v37, v40, v39
	v_fmac_f32_e32 v40, v41, v38
	v_fma_f32 v37, -v37, v40, v39
	v_div_fmas_f32 v37, v37, v38, v40
	v_div_fixup_f32 v36, v37, v36, s13
	v_cndmask_b32_e64 v38, 1.0, v36, s[0:1]
	v_mul_f32_e32 v9, v9, v38
	v_mul_f32_e32 v13, v13, v38
	v_mul_f32_e32 v8, v8, v38
	v_mul_f32_e32 v6, v6, v38
	v_mul_f32_e32 v7, v7, v38
	v_rndne_f32_e32 v9, v9
	v_mul_f32_e32 v12, v12, v38
	v_mul_f32_e32 v10, v10, v38
	v_mul_f32_e32 v11, v11, v38
	v_rndne_f32_e32 v13, v13
	v_rndne_f32_e32 v8, v8
	v_cvt_i32_f32_e32 v9, v9
	v_rndne_f32_e32 v6, v6
	v_rndne_f32_e32 v7, v7
	v_rndne_f32_e32 v12, v12
	v_cvt_i32_f32_e32 v13, v13
	v_rndne_f32_e32 v10, v10
	v_rndne_f32_e32 v11, v11
	v_cvt_i32_f32_e32 v8, v8
	v_cvt_i32_f32_sdwa v6, v6 dst_sel:WORD_1 dst_unused:UNUSED_PAD src0_sel:DWORD
	v_cvt_i32_f32_e32 v7, v7
	v_cvt_i32_f32_e32 v12, v12
	v_cvt_i32_f32_sdwa v10, v10 dst_sel:WORD_1 dst_unused:UNUSED_PAD src0_sel:DWORD
	v_cvt_i32_f32_e32 v11, v11
	s_add_u32 s0, s70, s2
	s_addc_u32 s1, s71, s3
	v_lshlrev_b32_e32 v9, 8, v9
	v_lshl_add_u64 v[36:37], s[0:1], 0, v[148:149]
	v_lshlrev_b32_e32 v13, 8, v13
	v_and_b32_e32 v9, 0xff00, v9
	v_and_b32_e32 v6, 0xff0000, v6
	v_perm_b32 v7, v7, v8, s57
	v_lshl_add_u64 v[36:37], v[36:37], 0, v[150:151]
	v_and_b32_e32 v13, 0xff00, v13
	v_and_b32_e32 v10, 0xff0000, v10
	v_perm_b32 v11, v11, v12, s57
	v_or3_b32 v6, v7, v9, v6
	v_or3_b32 v10, v11, v13, v10
	global_store_dword v[36:37], v6, off offset:2160
	v_lshl_add_u64 v[6:7], s[0:1], 0, v[44:45]
	global_store_dword v[36:37], v10, off offset:2144
	v_lshl_add_u64 v[10:11], v[6:7], 0, v[42:43]
	v_mul_f32_e32 v7, v67, v38
	v_mul_f32_e32 v6, v62, v38
	v_mul_f32_e32 v8, v71, v38
	v_mul_f32_e32 v9, v75, v38
	v_rndne_f32_e32 v7, v7
	v_rndne_f32_e32 v6, v6
	v_cvt_i32_f32_e32 v7, v7
	v_rndne_f32_e32 v8, v8
	v_rndne_f32_e32 v9, v9
	v_cvt_i32_f32_e32 v6, v6
	v_cvt_i32_f32_sdwa v8, v8 dst_sel:WORD_1 dst_unused:UNUSED_PAD src0_sel:DWORD
	v_cvt_i32_f32_e32 v9, v9
	v_lshlrev_b32_e32 v7, 8, v7
	v_and_b32_e32 v7, 0xff00, v7
	v_and_b32_e32 v8, 0xff0000, v8
	v_perm_b32 v6, v9, v6, s57
	v_or3_b32 v6, v6, v7, v8
	v_mul_f32_e32 v8, v66, v38
	v_mul_f32_e32 v7, v32, v38
	v_mul_f32_e32 v9, v70, v38
	v_mul_f32_e32 v12, v74, v38
	v_rndne_f32_e32 v8, v8
	v_rndne_f32_e32 v7, v7
	v_cvt_i32_f32_e32 v8, v8
	v_rndne_f32_e32 v9, v9
	v_rndne_f32_e32 v12, v12
	v_cvt_i32_f32_e32 v7, v7
	v_cvt_i32_f32_sdwa v9, v9 dst_sel:WORD_1 dst_unused:UNUSED_PAD src0_sel:DWORD
	v_cvt_i32_f32_e32 v12, v12
	v_lshlrev_b32_e32 v8, 8, v8
	v_and_b32_e32 v8, 0xff00, v8
	v_and_b32_e32 v9, 0xff0000, v9
	v_perm_b32 v7, v12, v7, s57
	v_mul_f32_e32 v17, v17, v38
	v_or3_b32 v7, v7, v8, v9
	v_mul_f32_e32 v9, v65, v38
	v_mul_f32_e32 v16, v16, v38
	v_mul_f32_e32 v14, v14, v38
	v_mul_f32_e32 v15, v15, v38
	v_rndne_f32_e32 v17, v17
	v_mul_f32_e32 v8, v31, v38
	v_mul_f32_e32 v12, v69, v38
	v_mul_f32_e32 v13, v73, v38
	v_rndne_f32_e32 v9, v9
	v_rndne_f32_e32 v16, v16
	v_cvt_i32_f32_e32 v17, v17
	v_rndne_f32_e32 v14, v14
	v_rndne_f32_e32 v15, v15
	v_rndne_f32_e32 v8, v8
	v_cvt_i32_f32_e32 v9, v9
	v_rndne_f32_e32 v12, v12
	v_rndne_f32_e32 v13, v13
	v_cvt_i32_f32_e32 v16, v16
	v_cvt_i32_f32_sdwa v14, v14 dst_sel:WORD_1 dst_unused:UNUSED_PAD src0_sel:DWORD
	v_cvt_i32_f32_e32 v15, v15
	v_cvt_i32_f32_e32 v8, v8
	v_cvt_i32_f32_sdwa v12, v12 dst_sel:WORD_1 dst_unused:UNUSED_PAD src0_sel:DWORD
	v_cvt_i32_f32_e32 v13, v13
	v_lshlrev_b32_e32 v17, 8, v17
	v_lshlrev_b32_e32 v9, 8, v9
	v_and_b32_e32 v17, 0xff00, v17
	v_and_b32_e32 v14, 0xff0000, v14
	v_perm_b32 v15, v15, v16, s57
	v_and_b32_e32 v9, 0xff00, v9
	v_and_b32_e32 v12, 0xff0000, v12
	v_perm_b32 v8, v13, v8, s57
	v_or3_b32 v14, v15, v17, v14
	v_or3_b32 v8, v8, v9, v12
	v_mul_f32_e32 v12, v63, v38
	global_store_dword v[36:37], v14, off offset:2128
	v_mul_f32_e32 v9, v29, v38
	v_mul_f32_e32 v13, v68, v38
	v_mul_f32_e32 v14, v72, v38
	v_rndne_f32_e32 v12, v12
	v_rndne_f32_e32 v9, v9
	v_cvt_i32_f32_e32 v12, v12
	v_rndne_f32_e32 v13, v13
	v_rndne_f32_e32 v14, v14
	v_cvt_i32_f32_e32 v9, v9
	v_cvt_i32_f32_sdwa v13, v13 dst_sel:WORD_1 dst_unused:UNUSED_PAD src0_sel:DWORD
	v_cvt_i32_f32_e32 v14, v14
	v_lshlrev_b32_e32 v12, 8, v12
	v_and_b32_e32 v12, 0xff00, v12
	v_and_b32_e32 v13, 0xff0000, v13
	v_perm_b32 v9, v14, v9, s57
	v_or3_b32 v9, v9, v12, v13
	v_mul_f32_e32 v40, v61, v38
	global_store_dwordx4 v[10:11], v[6:9], off
	v_mul_f32_e32 v39, v60, v38
	v_mul_f32_e32 v41, v58, v38
	v_mul_f32_e32 v7, v27, v38
	v_mul_f32_e32 v58, v59, v38
	v_rndne_f32_e32 v40, v40
	v_mul_f32_e32 v6, v24, v38
	v_mul_f32_e32 v8, v30, v38
	v_mul_f32_e32 v9, v64, v38
	v_rndne_f32_e32 v7, v7
	v_rndne_f32_e32 v39, v39
	v_cvt_i32_f32_e32 v40, v40
	v_rndne_f32_e32 v41, v41
	v_rndne_f32_e32 v58, v58
	v_rndne_f32_e32 v6, v6
	v_cvt_i32_f32_e32 v7, v7
	v_rndne_f32_e32 v8, v8
	v_rndne_f32_e32 v9, v9
	v_cvt_i32_f32_e32 v39, v39
	v_cvt_i32_f32_sdwa v41, v41 dst_sel:WORD_1 dst_unused:UNUSED_PAD src0_sel:DWORD
	v_cvt_i32_f32_e32 v58, v58
	v_cvt_i32_f32_e32 v6, v6
	v_cvt_i32_f32_sdwa v8, v8 dst_sel:WORD_1 dst_unused:UNUSED_PAD src0_sel:DWORD
	v_cvt_i32_f32_e32 v9, v9
	v_lshlrev_b32_e32 v40, 8, v40
	v_lshlrev_b32_e32 v7, 8, v7
	v_and_b32_e32 v40, 0xff00, v40
	v_and_b32_e32 v41, 0xff0000, v41
	v_perm_b32 v39, v58, v39, s57
	v_and_b32_e32 v7, 0xff00, v7
	v_and_b32_e32 v8, 0xff0000, v8
	v_perm_b32 v6, v9, v6, s57
	v_or3_b32 v39, v39, v40, v41
	v_mul_f32_e32 v40, v57, v38
	v_or3_b32 v6, v6, v7, v8
	v_mul_f32_e32 v8, v26, v38
	global_store_dword v[36:37], v39, off offset:2048
	v_mul_f32_e32 v39, v56, v38
	v_mul_f32_e32 v41, v54, v38
	v_mul_f32_e32 v54, v55, v38
	v_rndne_f32_e32 v40, v40
	v_mul_f32_e32 v7, v23, v38
	v_mul_f32_e32 v9, v28, v38
	v_mul_f32_e32 v12, v33, v38
	v_rndne_f32_e32 v8, v8
	v_rndne_f32_e32 v39, v39
	v_cvt_i32_f32_e32 v40, v40
	v_rndne_f32_e32 v41, v41
	v_rndne_f32_e32 v54, v54
	v_rndne_f32_e32 v7, v7
	v_cvt_i32_f32_e32 v8, v8
	v_rndne_f32_e32 v9, v9
	v_rndne_f32_e32 v12, v12
	v_cvt_i32_f32_e32 v39, v39
	v_cvt_i32_f32_sdwa v41, v41 dst_sel:WORD_1 dst_unused:UNUSED_PAD src0_sel:DWORD
	v_cvt_i32_f32_e32 v54, v54
	v_cvt_i32_f32_e32 v7, v7
	v_cvt_i32_f32_sdwa v9, v9 dst_sel:WORD_1 dst_unused:UNUSED_PAD src0_sel:DWORD
	v_cvt_i32_f32_e32 v12, v12
	v_lshlrev_b32_e32 v40, 8, v40
	v_lshlrev_b32_e32 v8, 8, v8
	v_and_b32_e32 v40, 0xff00, v40
	v_and_b32_e32 v41, 0xff0000, v41
	v_perm_b32 v39, v54, v39, s57
	v_and_b32_e32 v8, 0xff00, v8
	v_and_b32_e32 v9, 0xff0000, v9
	v_perm_b32 v7, v12, v7, s57
	v_or3_b32 v39, v39, v40, v41
	v_mul_f32_e32 v40, v53, v38
	v_or3_b32 v7, v7, v8, v9
	v_mul_f32_e32 v9, v25, v38
	global_store_dword v[36:37], v39, off offset:2064
	v_mul_f32_e32 v39, v52, v38
	v_mul_f32_e32 v41, v50, v38
	v_mul_f32_e32 v50, v51, v38
	v_rndne_f32_e32 v40, v40
	v_mul_f32_e32 v8, v22, v38
	v_mul_f32_e32 v2, v2, v38
	v_mul_f32_e32 v12, v34, v38
	v_rndne_f32_e32 v9, v9
	v_rndne_f32_e32 v39, v39
	v_cvt_i32_f32_e32 v40, v40
	v_rndne_f32_e32 v41, v41
	v_rndne_f32_e32 v50, v50
	v_rndne_f32_e32 v8, v8
	v_cvt_i32_f32_e32 v9, v9
	v_rndne_f32_e32 v2, v2
	v_rndne_f32_e32 v12, v12
	v_cvt_i32_f32_e32 v39, v39
	v_cvt_i32_f32_sdwa v41, v41 dst_sel:WORD_1 dst_unused:UNUSED_PAD src0_sel:DWORD
	v_cvt_i32_f32_e32 v50, v50
	v_cvt_i32_f32_e32 v8, v8
	v_cvt_i32_f32_sdwa v2, v2 dst_sel:WORD_1 dst_unused:UNUSED_PAD src0_sel:DWORD
	v_cvt_i32_f32_e32 v12, v12
	v_lshlrev_b32_e32 v40, 8, v40
	v_lshlrev_b32_e32 v9, 8, v9
	v_and_b32_e32 v40, 0xff00, v40
	v_and_b32_e32 v41, 0xff0000, v41
	v_perm_b32 v39, v50, v39, s57
	v_and_b32_e32 v9, 0xff00, v9
	v_and_b32_e32 v2, 0xff0000, v2
	v_perm_b32 v8, v12, v8, s57
	v_or3_b32 v39, v39, v40, v41
	v_mul_f32_e32 v40, v49, v38
	v_mul_f32_e32 v19, v19, v38
	v_or3_b32 v8, v8, v9, v2
	v_mul_f32_e32 v2, v3, v38
	v_mul_f32_e32 v3, v4, v38
	global_store_dword v[36:37], v39, off offset:2080
	v_mul_f32_e32 v39, v48, v38
	v_mul_f32_e32 v41, v46, v38
	v_mul_f32_e32 v46, v47, v38
	v_rndne_f32_e32 v40, v40
	v_mul_f32_e32 v18, v18, v38
	v_mul_f32_e32 v20, v20, v38
	v_mul_f32_e32 v21, v21, v38
	v_rndne_f32_e32 v19, v19
	v_mul_f32_e32 v4, v35, v38
	v_mul_f32_e32 v5, v5, v38
	v_rndne_f32_e32 v3, v3
	v_rndne_f32_e32 v39, v39
	v_cvt_i32_f32_e32 v40, v40
	v_rndne_f32_e32 v41, v41
	v_rndne_f32_e32 v46, v46
	v_rndne_f32_e32 v18, v18
	v_cvt_i32_f32_e32 v19, v19
	v_rndne_f32_e32 v20, v20
	v_rndne_f32_e32 v21, v21
	v_rndne_f32_e32 v2, v2
	v_cvt_i32_f32_e32 v3, v3
	v_rndne_f32_e32 v4, v4
	v_rndne_f32_e32 v5, v5
	v_cvt_i32_f32_e32 v39, v39
	v_cvt_i32_f32_sdwa v41, v41 dst_sel:WORD_1 dst_unused:UNUSED_PAD src0_sel:DWORD
	v_cvt_i32_f32_e32 v46, v46
	v_cvt_i32_f32_e32 v18, v18
	v_cvt_i32_f32_sdwa v20, v20 dst_sel:WORD_1 dst_unused:UNUSED_PAD src0_sel:DWORD
	v_cvt_i32_f32_e32 v21, v21
	v_cvt_i32_f32_e32 v2, v2
	v_cvt_i32_f32_sdwa v4, v4 dst_sel:WORD_1 dst_unused:UNUSED_PAD src0_sel:DWORD
	v_cvt_i32_f32_e32 v5, v5
	v_lshlrev_b32_e32 v40, 8, v40
	v_lshlrev_b32_e32 v19, 8, v19
	v_lshlrev_b32_e32 v3, 8, v3
	v_and_b32_e32 v40, 0xff00, v40
	v_and_b32_e32 v41, 0xff0000, v41
	v_perm_b32 v39, v46, v39, s57
	v_and_b32_e32 v19, 0xff00, v19
	v_and_b32_e32 v20, 0xff0000, v20
	v_perm_b32 v18, v21, v18, s57
	v_and_b32_e32 v3, 0xff00, v3
	v_and_b32_e32 v4, 0xff0000, v4
	v_perm_b32 v2, v5, v2, s57
	v_or3_b32 v39, v39, v40, v41
	v_or3_b32 v18, v18, v19, v20
	v_or3_b32 v9, v2, v3, v4
	global_store_dword v[36:37], v39, off offset:2096
	global_store_dword v[36:37], v18, off offset:2112
	global_store_dwordx4 v[10:11], v[6:9], off offset:16
	v_readlane_b32 s0, v242, 33
	v_lshlrev_b32_e32 v4, 4, v78
	v_lshlrev_b32_e32 v2, 2, v78
	v_ashrrev_i32_e32 v5, 31, v4
	v_readlane_b32 s1, v242, 34
	s_lshl_b32 s6, s14, 1
	s_add_i32 s14, s14, 1
	v_lshl_add_u64 v[68:69], s[0:1], 0, v[4:5]
	v_lshlrev_b32_e32 v4, 3, v78
	v_and_b32_e32 v5, 60, v2
	s_movk_i32 s0, 0xff80
	v_and_or_b32 v4, v4, s0, v5
	v_readlane_b32 s0, v242, 31
	v_ashrrev_i32_e32 v3, 31, v2
	v_ashrrev_i32_e32 v5, 31, v4
	v_readlane_b32 s1, v242, 32
	s_lshl_b32 s7, s14, 1
	v_lshl_add_u64 v[66:67], v[2:3], 2, s[48:49]
	v_cmp_eq_u32_e64 s[2:3], 0, v78
	v_lshl_add_u64 v[70:71], v[4:5], 2, s[46:47]
	v_lshl_add_u64 v[72:73], s[0:1], 0, v[2:3]
	s_add_i32 s30, s42, s40
	s_cmp_gt_i32 s30, 0x3fff
	s_cbranch_scc1 .Lcv_b_nop
	s_waitcnt vmcnt(0)
	v_pk_mul_f32 v[50:51], v[180:181], v[180:181]
	v_pk_mul_f32 v[52:53], v[182:183], v[182:183]
	v_pk_fma_f32 v[50:51], v[184:185], v[184:185], v[50:51]
	v_pk_fma_f32 v[52:53], v[186:187], v[186:187], v[52:53]
	v_pk_fma_f32 v[50:51], v[188:189], v[188:189], v[50:51]
	v_pk_fma_f32 v[52:53], v[190:191], v[190:191], v[52:53]
	v_pk_fma_f32 v[50:51], v[192:193], v[192:193], v[50:51]
	v_pk_fma_f32 v[52:53], v[194:195], v[194:195], v[52:53]
	v_pk_fma_f32 v[50:51], v[196:197], v[196:197], v[50:51]
	v_pk_fma_f32 v[52:53], v[198:199], v[198:199], v[52:53]
	v_pk_fma_f32 v[50:51], v[200:201], v[200:201], v[50:51]
	v_pk_fma_f32 v[52:53], v[202:203], v[202:203], v[52:53]
	v_pk_fma_f32 v[50:51], v[204:205], v[204:205], v[50:51]
	v_pk_fma_f32 v[52:53], v[206:207], v[206:207], v[52:53]
	v_pk_fma_f32 v[50:51], v[208:209], v[208:209], v[50:51]
	v_pk_fma_f32 v[52:53], v[210:211], v[210:211], v[52:53]
	v_pk_fma_f32 v[50:51], v[212:213], v[212:213], v[50:51]
	v_pk_fma_f32 v[52:53], v[214:215], v[214:215], v[52:53]
	v_pk_fma_f32 v[50:51], v[216:217], v[216:217], v[50:51]
	v_pk_fma_f32 v[52:53], v[218:219], v[218:219], v[52:53]
	v_pk_fma_f32 v[50:51], v[220:221], v[220:221], v[50:51]
	v_pk_fma_f32 v[52:53], v[222:223], v[222:223], v[52:53]
	v_pk_fma_f32 v[50:51], v[224:225], v[224:225], v[50:51]
	v_pk_fma_f32 v[52:53], v[226:227], v[226:227], v[52:53]
	v_pk_fma_f32 v[50:51], v[228:229], v[228:229], v[50:51]
	v_pk_fma_f32 v[52:53], v[230:231], v[230:231], v[52:53]
	v_pk_fma_f32 v[50:51], v[232:233], v[232:233], v[50:51]
	v_pk_fma_f32 v[52:53], v[234:235], v[234:235], v[52:53]
	v_pk_fma_f32 v[50:51], v[236:237], v[236:237], v[50:51]
	v_pk_fma_f32 v[52:53], v[238:239], v[238:239], v[52:53]
	v_pk_fma_f32 v[50:51], v[134:135], v[134:135], v[50:51]
	v_pk_fma_f32 v[52:53], v[136:137], v[136:137], v[52:53]
	v_pk_add_f32 v[50:51], v[50:51], v[52:53]
	v_add_f32_e32 v54, v50, v51
	s_nop 1
	v_add_f32_dpp v54, v54, v54 quad_perm:[1,0,3,2] row_mask:0xf bank_mask:0xf bound_ctrl:1
	s_nop 1
	v_add_f32_dpp v54, v54, v54 quad_perm:[2,3,0,1] row_mask:0xf bank_mask:0xf bound_ctrl:1
	s_nop 1
	v_add_f32_dpp v54, v54, v54 row_half_mirror row_mask:0xf bank_mask:0xf bound_ctrl:1
	s_nop 1
	v_add_f32_dpp v54, v54, v54 row_mirror row_mask:0xf bank_mask:0xf bound_ctrl:1
	s_nop 1
	v_add_f32_dpp v54, v54, v54 row_bcast:15 row_mask:0xa bank_mask:0xf
	s_nop 1
	v_add_f32_dpp v54, v54, v54 row_bcast:31 row_mask:0xc bank_mask:0xf
	s_nop 1
	v_readlane_b32 s22, v54, 63
	s_lshl_b32 s24, s30, 11
	v_readlane_b32 s26, v242, 33
	v_readlane_b32 s27, v242, 34
	s_add_u32 s23, s30, 0x4000
	s_lshl_b32 s23, s23, 2
	v_mov_b32_e32 v56, s22
	v_mul_f32_e32 v56, 0x39800000, v56
	v_sqrt_f32_e32 v56, v56
	v_cmp_lt_f32_e64 s[28:29], 0, s22
	v_mul_f32_e32 v56, 0x3eddddde, v56
	s_add_u32 s26, s26, s24
	s_addc_u32 s27, s27, 0
	v_cndmask_b32_e64 v56, 1.0, v56, s[28:29]
	s_add_u32 s24, s74, s23
	s_addc_u32 s25, s75, 0
	v_rcp_f32_e32 v58, v56
	v_mov_b32_e32 v54, 0
	v_fma_f32 v59, -v56, v58, 1.0
	v_fmac_f32_e32 v58, v59, v58
	s_mov_b64 exec, 1
	global_store_dword v54, v56, s[24:25]
	s_mov_b64 exec, -1
	v_lshlrev_b32_e32 v138, 4, v1
	v_pk_mul_f32 v[180:181], v[180:181], v[58:59] op_sel_hi:[1,0]
	v_pk_mul_f32 v[182:183], v[182:183], v[58:59] op_sel_hi:[1,0]
	v_pk_mul_f32 v[184:185], v[184:185], v[58:59] op_sel_hi:[1,0]
	v_pk_mul_f32 v[186:187], v[186:187], v[58:59] op_sel_hi:[1,0]
	v_pk_mul_f32 v[188:189], v[188:189], v[58:59] op_sel_hi:[1,0]
	v_pk_mul_f32 v[190:191], v[190:191], v[58:59] op_sel_hi:[1,0]
	v_pk_mul_f32 v[192:193], v[192:193], v[58:59] op_sel_hi:[1,0]
	v_pk_mul_f32 v[194:195], v[194:195], v[58:59] op_sel_hi:[1,0]
	v_pk_mul_f32 v[196:197], v[196:197], v[58:59] op_sel_hi:[1,0]
	v_pk_mul_f32 v[198:199], v[198:199], v[58:59] op_sel_hi:[1,0]
	v_pk_mul_f32 v[200:201], v[200:201], v[58:59] op_sel_hi:[1,0]
	v_pk_mul_f32 v[202:203], v[202:203], v[58:59] op_sel_hi:[1,0]
	v_pk_mul_f32 v[204:205], v[204:205], v[58:59] op_sel_hi:[1,0]
	v_pk_mul_f32 v[206:207], v[206:207], v[58:59] op_sel_hi:[1,0]
	v_pk_mul_f32 v[208:209], v[208:209], v[58:59] op_sel_hi:[1,0]
	v_pk_mul_f32 v[210:211], v[210:211], v[58:59] op_sel_hi:[1,0]
	v_pk_mul_f32 v[212:213], v[212:213], v[58:59] op_sel_hi:[1,0]
	v_pk_mul_f32 v[214:215], v[214:215], v[58:59] op_sel_hi:[1,0]
	v_pk_mul_f32 v[216:217], v[216:217], v[58:59] op_sel_hi:[1,0]
	v_pk_mul_f32 v[218:219], v[218:219], v[58:59] op_sel_hi:[1,0]
	v_pk_mul_f32 v[220:221], v[220:221], v[58:59] op_sel_hi:[1,0]
	v_pk_mul_f32 v[222:223], v[222:223], v[58:59] op_sel_hi:[1,0]
	v_pk_mul_f32 v[224:225], v[224:225], v[58:59] op_sel_hi:[1,0]
	v_pk_mul_f32 v[226:227], v[226:227], v[58:59] op_sel_hi:[1,0]
	v_pk_mul_f32 v[228:229], v[228:229], v[58:59] op_sel_hi:[1,0]
	v_pk_mul_f32 v[230:231], v[230:231], v[58:59] op_sel_hi:[1,0]
	v_pk_mul_f32 v[232:233], v[232:233], v[58:59] op_sel_hi:[1,0]
	v_pk_mul_f32 v[234:235], v[234:235], v[58:59] op_sel_hi:[1,0]
	v_pk_mul_f32 v[236:237], v[236:237], v[58:59] op_sel_hi:[1,0]
	v_pk_mul_f32 v[238:239], v[238:239], v[58:59] op_sel_hi:[1,0]
	v_pk_mul_f32 v[134:135], v[134:135], v[58:59] op_sel_hi:[1,0]
	v_pk_mul_f32 v[136:137], v[136:137], v[58:59] op_sel_hi:[1,0]
	v_cvt_scalef32_pk_fp4_f32 v60, v180, v181, 1.0
	v_cvt_scalef32_pk_fp4_f32 v61, v188, v189, 1.0
	v_cvt_scalef32_pk_fp4_f32 v62, v196, v197, 1.0
	v_cvt_scalef32_pk_fp4_f32 v63, v204, v205, 1.0
	v_cvt_scalef32_pk_fp4_f32 v60, v182, v183, 1.0 op_sel:[0,0,1,0]
	v_cvt_scalef32_pk_fp4_f32 v61, v190, v191, 1.0 op_sel:[0,0,1,0]
	v_cvt_scalef32_pk_fp4_f32 v62, v198, v199, 1.0 op_sel:[0,0,1,0]
	v_cvt_scalef32_pk_fp4_f32 v63, v206, v207, 1.0 op_sel:[0,0,1,0]
	v_cvt_scalef32_pk_fp4_f32 v60, v184, v185, 1.0 op_sel:[0,0,0,1]
	v_cvt_scalef32_pk_fp4_f32 v61, v192, v193, 1.0 op_sel:[0,0,0,1]
	v_cvt_scalef32_pk_fp4_f32 v62, v200, v201, 1.0 op_sel:[0,0,0,1]
	v_cvt_scalef32_pk_fp4_f32 v63, v208, v209, 1.0 op_sel:[0,0,0,1]
	v_cvt_scalef32_pk_fp4_f32 v60, v186, v187, 1.0 op_sel:[0,0,1,1]
	v_cvt_scalef32_pk_fp4_f32 v61, v194, v195, 1.0 op_sel:[0,0,1,1]
	v_cvt_scalef32_pk_fp4_f32 v62, v202, v203, 1.0 op_sel:[0,0,1,1]
	v_cvt_scalef32_pk_fp4_f32 v63, v210, v211, 1.0 op_sel:[0,0,1,1]
	s_nop 0
	global_store_dwordx4 v138, v[60:63], s[26:27]
	s_nop 1
	v_cvt_scalef32_pk_fp4_f32 v60, v212, v213, 1.0
	v_cvt_scalef32_pk_fp4_f32 v61, v220, v221, 1.0
	v_cvt_scalef32_pk_fp4_f32 v62, v228, v229, 1.0
	v_cvt_scalef32_pk_fp4_f32 v63, v236, v237, 1.0
	v_cvt_scalef32_pk_fp4_f32 v60, v214, v215, 1.0 op_sel:[0,0,1,0]
	v_cvt_scalef32_pk_fp4_f32 v61, v222, v223, 1.0 op_sel:[0,0,1,0]
	v_cvt_scalef32_pk_fp4_f32 v62, v230, v231, 1.0 op_sel:[0,0,1,0]
	v_cvt_scalef32_pk_fp4_f32 v63, v238, v239, 1.0 op_sel:[0,0,1,0]
	v_cvt_scalef32_pk_fp4_f32 v60, v216, v217, 1.0 op_sel:[0,0,0,1]
	v_cvt_scalef32_pk_fp4_f32 v61, v224, v225, 1.0 op_sel:[0,0,0,1]
	v_cvt_scalef32_pk_fp4_f32 v62, v232, v233, 1.0 op_sel:[0,0,0,1]
	v_cvt_scalef32_pk_fp4_f32 v63, v134, v135, 1.0 op_sel:[0,0,0,1]
	v_cvt_scalef32_pk_fp4_f32 v60, v218, v219, 1.0 op_sel:[0,0,1,1]
	v_cvt_scalef32_pk_fp4_f32 v61, v226, v227, 1.0 op_sel:[0,0,1,1]
	v_cvt_scalef32_pk_fp4_f32 v62, v234, v235, 1.0 op_sel:[0,0,1,1]
	v_cvt_scalef32_pk_fp4_f32 v63, v136, v137, 1.0 op_sel:[0,0,1,1]
	s_nop 0
	global_store_dwordx4 v138, v[60:63], s[26:27] offset:1024
.Lcv_b_nop:
	s_branch .LBB0_519
.LBB0_1140:
	v_readlane_b32 s78, v242, 46
	v_readlane_b32 s44, v242, 0
	v_readlane_b32 s60, v242, 7
	v_readlane_b32 s20, v242, 43
	v_readlane_b32 s77, v242, 48
	v_readlane_b32 s97, v242, 50
	v_readlane_b32 s79, v242, 47
	v_readlane_b32 s76, v242, 49
	v_readlane_b32 s45, v242, 1
	v_readlane_b32 s96, v242, 45
	v_readlane_b32 s61, v242, 8
	v_readlane_b32 s21, v242, 44
	v_readlane_b32 s22, v242, 51
	v_readlane_b32 s23, v242, 52
